# baseline (speedup 1.0000x reference)
_Z9ssim_mainPKfS0_S0_Pf:
	v_readfirstlane_b32 s29, v0
	s_load_dwordx4 s[4:7], s[0:1], 0x0
	s_load_dwordx4 s[8:11], s[0:1], 0x10
	s_mov_b32 s51, 0x44800000
	s_mov_b32 s38, 0
	s_mov_b32 s39, -1
	s_lshr_b32 s12, s29, 6
	s_and_b32 s13, s2, 7
	s_lshl_b32 s13, s13, 5
	s_lshr_b32 s14, s2, 3
	s_add_u32 s13, s13, s14
	s_lshr_b32 s14, s13, 3
	s_and_b32 s15, s13, 7
	s_lshl_b32 s16, s14, 20
	s_lshl_b32 s17, s15, 17
	s_add_u32 s16, s16, s17
	s_lshl_b32 s17, s12, 8
	s_add_u32 s16, s16, s17
	s_lshl_b32 s27, s12, 2
	s_add_u32 s27, s27, 0x10000
	v_and_b32_e32 v8, 63, v0
	v_and_b32_e32 v169, 15, v0
	v_bfe_u32 v164, v0, 4, 2
	v_lshrrev_b32_e32 v167, 2, v169
	v_lshlrev_b32_e32 v167, 5, v167
	v_and_b32_e32 v168, 1, v169
	v_lshl_or_b32 v167, v168, 4, v167
	v_bfe_u32 v168, v169, 1, 1
	v_lshl_or_b32 v167, v168, 7, v167
	v_lshl_or_b32 v9, v164, 14, v167
	v_and_b32_e32 v168, 1, v164
	v_lshl_or_b32 v23, v168, 14, v167
	v_lshrrev_b32_e32 v168, 1, v164
	v_lshl_or_b32 v23, v168, 13, v23
	v_add_u32_e32 v237, 0x1000, v9
	v_add_u32_e32 v238, 0x2000, v9
	v_add_u32_e32 v239, 0x3000, v9
	v_add_u32_e32 v240, 0x10000, v9
	v_add_u32_e32 v241, 0x11000, v9
	v_add_u32_e32 v242, 0x12000, v9
	v_add_u32_e32 v243, 0x13000, v9
	s_waitcnt lgkmcnt(0)
	s_load_dwordx8 s[40:47], s[8:9], 0x0
	s_load_dwordx2 s[48:49], s[8:9], 0x20
	s_load_dword s50, s[8:9], 0x28
	s_add_u32 s18, s4, s16
	s_addc_u32 s19, s5, 0
	s_add_u32 s20, s6, s16
	s_addc_u32 s21, s7, 0
	s_cmp_lt_u32 s12, 4
	s_cbranch_scc1 .Lq_noc0dly
	s_sleep 4
.Lq_noc0dly:
	global_load_dwordx4 v[36:39], v9, s[18:19] offset:0 sc1 nt
	global_load_dwordx4 v[40:43], v9, s[18:19] offset:2048 sc1 nt
	global_load_dwordx4 v[68:71], v9, s[20:21] offset:0 sc1 nt
	global_load_dwordx4 v[72:75], v9, s[20:21] offset:2048 sc1 nt
	global_load_dwordx4 v[44:47], v237, s[18:19] offset:0 sc1 nt
	global_load_dwordx4 v[48:51], v237, s[18:19] offset:2048 sc1 nt
	global_load_dwordx4 v[76:79], v237, s[20:21] offset:0 sc1 nt
	global_load_dwordx4 v[80:83], v237, s[20:21] offset:2048 sc1 nt
	global_load_dwordx4 v[52:55], v238, s[18:19] offset:0 sc1 nt
	global_load_dwordx4 v[56:59], v238, s[18:19] offset:2048 sc1 nt
	global_load_dwordx4 v[84:87], v238, s[20:21] offset:0 sc1 nt
	global_load_dwordx4 v[88:91], v238, s[20:21] offset:2048 sc1 nt
	global_load_dwordx4 v[60:63], v239, s[18:19] offset:0 sc1 nt
	global_load_dwordx4 v[64:67], v239, s[18:19] offset:2048 sc1 nt
	global_load_dwordx4 v[92:95], v239, s[20:21] offset:0 sc1 nt
	global_load_dwordx4 v[96:99], v239, s[20:21] offset:2048 sc1 nt
	v_mov_b32_e32 v6, s27
	v_mov_b32_e32 v168, 0
	ds_write_b32 v6, v168 offset:0
	ds_write_b32 v6, v168 offset:32
	ds_write_b32 v6, v168 offset:64
	ds_write_b32 v6, v168 offset:96
	v_lshlrev_b32_e32 v167, 3, v164
	v_xor_b32_e32 v168, 16, v167
	v_sub_u32_e32 v165, v167, v169
	v_sub_u32_e32 v166, v168, v169
	v_add_u32_e32 v172, 0, v165
	v_min_u32_e32 v172, 11, v172
	v_lshlrev_b32_e32 v172, 2, v172
	v_add_u32_e32 v173, 1, v165
	v_min_u32_e32 v173, 11, v173
	v_lshlrev_b32_e32 v173, 2, v173
	v_add_u32_e32 v174, 2, v165
	v_min_u32_e32 v174, 11, v174
	v_lshlrev_b32_e32 v174, 2, v174
	v_add_u32_e32 v175, 3, v165
	v_min_u32_e32 v175, 11, v175
	v_lshlrev_b32_e32 v175, 2, v175
	v_add_u32_e32 v176, 4, v165
	v_min_u32_e32 v176, 11, v176
	v_lshlrev_b32_e32 v176, 2, v176
	v_add_u32_e32 v177, 5, v165
	v_min_u32_e32 v177, 11, v177
	v_lshlrev_b32_e32 v177, 2, v177
	v_add_u32_e32 v178, 6, v165
	v_min_u32_e32 v178, 11, v178
	v_lshlrev_b32_e32 v178, 2, v178
	v_add_u32_e32 v179, 7, v165
	v_min_u32_e32 v179, 11, v179
	v_lshlrev_b32_e32 v179, 2, v179
	v_add_u32_e32 v180, 0, v166
	v_min_u32_e32 v180, 11, v180
	v_lshlrev_b32_e32 v180, 2, v180
	v_add_u32_e32 v181, 1, v166
	v_min_u32_e32 v181, 11, v181
	v_lshlrev_b32_e32 v181, 2, v181
	v_add_u32_e32 v182, 2, v166
	v_min_u32_e32 v182, 11, v182
	v_lshlrev_b32_e32 v182, 2, v182
	v_add_u32_e32 v183, 3, v166
	v_min_u32_e32 v183, 11, v183
	v_lshlrev_b32_e32 v183, 2, v183
	v_add_u32_e32 v184, 4, v166
	v_min_u32_e32 v184, 11, v184
	v_lshlrev_b32_e32 v184, 2, v184
	v_add_u32_e32 v185, 5, v166
	v_min_u32_e32 v185, 11, v185
	v_lshlrev_b32_e32 v185, 2, v185
	v_add_u32_e32 v186, 6, v166
	v_min_u32_e32 v186, 11, v186
	v_lshlrev_b32_e32 v186, 2, v186
	v_add_u32_e32 v187, 7, v166
	v_min_u32_e32 v187, 11, v187
	v_lshlrev_b32_e32 v187, 2, v187
	s_cmp_eq_u32 s15, 7
	s_cselect_b32 s22, 0, 0x20000
	s_add_u32 s84, s18, s22
	s_addc_u32 s85, s19, 0
	s_add_u32 s86, s18, s22
	s_addc_u32 s87, s19, 0
	s_add_u32 s86, s86, 0x1000
	s_addc_u32 s87, s87, 0
	s_add_u32 s88, s20, s22
	s_addc_u32 s89, s21, 0
	s_add_u32 s90, s20, s22
	s_addc_u32 s91, s21, 0
	s_add_u32 s90, s90, 0x1000
	s_addc_u32 s91, s91, 0
	s_waitcnt lgkmcnt(0)
	v_writelane_b32 v171, s40, 0
	v_writelane_b32 v171, s41, 1
	v_writelane_b32 v171, s42, 2
	v_writelane_b32 v171, s43, 3
	v_writelane_b32 v171, s44, 4
	v_writelane_b32 v171, s45, 5
	v_writelane_b32 v171, s46, 6
	v_writelane_b32 v171, s47, 7
	v_writelane_b32 v171, s48, 8
	v_writelane_b32 v171, s49, 9
	v_writelane_b32 v171, s50, 10
	v_writelane_b32 v171, 0, 11
	v_fma_mixlo_f16 v171, v171, s51, 0
	ds_bpermute_b32 v188, v172, v171
	ds_bpermute_b32 v189, v173, v171
	ds_bpermute_b32 v190, v174, v171
	ds_bpermute_b32 v191, v175, v171
	ds_bpermute_b32 v192, v176, v171
	ds_bpermute_b32 v193, v177, v171
	ds_bpermute_b32 v194, v178, v171
	ds_bpermute_b32 v195, v179, v171
	v_mov_b32_e32 v229, 0x44800000
	v_fma_mixlo_f16 v228, s40, v229, 0
	v_cvt_f32_f16_e32 v228, v228
	v_cvt_f64_f32_e32 v[212:213], v228
	v_add_f64 v[212:213], v[212:213], 0
	v_fma_mixlo_f16 v228, s41, v229, 0
	v_cvt_f32_f16_e32 v228, v228
	v_cvt_f64_f32_e32 v[214:215], v228
	v_add_f64 v[212:213], v[212:213], v[214:215]
	v_fma_mixlo_f16 v228, s42, v229, 0
	v_cvt_f32_f16_e32 v228, v228
	v_cvt_f64_f32_e32 v[214:215], v228
	v_add_f64 v[212:213], v[212:213], v[214:215]
	v_fma_mixlo_f16 v228, s43, v229, 0
	v_cvt_f32_f16_e32 v228, v228
	v_cvt_f64_f32_e32 v[214:215], v228
	v_add_f64 v[212:213], v[212:213], v[214:215]
	v_fma_mixlo_f16 v228, s44, v229, 0
	v_cvt_f32_f16_e32 v228, v228
	v_cvt_f64_f32_e32 v[214:215], v228
	v_add_f64 v[212:213], v[212:213], v[214:215]
	v_fma_mixlo_f16 v228, s45, v229, 0
	v_cvt_f32_f16_e32 v228, v228
	v_cvt_f64_f32_e32 v[214:215], v228
	v_add_f64 v[212:213], v[212:213], v[214:215]
	v_fma_mixlo_f16 v228, s46, v229, 0
	v_cvt_f32_f16_e32 v228, v228
	v_cvt_f64_f32_e32 v[214:215], v228
	v_add_f64 v[212:213], v[212:213], v[214:215]
	v_fma_mixlo_f16 v228, s47, v229, 0
	v_cvt_f32_f16_e32 v228, v228
	v_cvt_f64_f32_e32 v[214:215], v228
	v_add_f64 v[212:213], v[212:213], v[214:215]
	v_fma_mixlo_f16 v228, s48, v229, 0
	v_cvt_f32_f16_e32 v228, v228
	v_cvt_f64_f32_e32 v[214:215], v228
	v_add_f64 v[212:213], v[212:213], v[214:215]
	v_fma_mixlo_f16 v228, s49, v229, 0
	v_cvt_f32_f16_e32 v228, v228
	v_cvt_f64_f32_e32 v[214:215], v228
	v_add_f64 v[212:213], v[212:213], v[214:215]
	v_fma_mixlo_f16 v228, s50, v229, 0
	v_cvt_f32_f16_e32 v228, v228
	v_cvt_f64_f32_e32 v[214:215], v228
	v_add_f64 v[212:213], v[212:213], v[214:215]
	s_waitcnt lgkmcnt(7)
	ds_bpermute_b32 v196, v180, v171
	ds_bpermute_b32 v197, v181, v171
	ds_bpermute_b32 v198, v182, v171
	ds_bpermute_b32 v199, v183, v171
	ds_bpermute_b32 v200, v184, v171
	ds_bpermute_b32 v201, v185, v171
	ds_bpermute_b32 v202, v186, v171
	ds_bpermute_b32 v203, v187, v171
	v_mul_f64 v[212:213], v[212:213], v[212:213]
	v_mul_f64 v[216:217], v[212:213], 0.5
	v_add_f64 v[218:219], v[216:217], v[216:217]
	s_mov_b32 s36, 0xeb1c432d
	s_mov_b32 s37, 0x3f1a36e2
	v_mul_f64 v[220:221], v[212:213], s[36:37]
	v_mul_f64 v[222:223], v[216:217], v[218:219]
	v_fmac_f64_e32 v[222:223], v[212:213], v[220:221]
	v_add_f64 v[224:225], v[212:213], v[212:213]
	s_mov_b32 s36, 0x487fcb92
	s_mov_b32 s37, 0x3f4d7dbf
	v_mul_f64 v[226:227], v[212:213], s[36:37]
	v_cvt_f32_f64_e32 v0, v[226:227]
	v_mov_b32_e32 v1, v0
	v_mov_b32_e32 v2, v0
	v_mov_b32_e32 v3, v0
	v_cvt_f32_f64_e32 v10, v[218:219]
	v_cvt_f32_f64_e32 v11, v[222:223]
	v_cvt_f32_f64_e32 v12, v[212:213]
	v_cvt_f32_f64_e32 v13, v[224:225]
	v_mul_f64 v[226:227], v[212:213], v[226:227]
	v_cvt_f32_f64_e32 v14, v[226:227]
	v_lshlrev_b32_e32 v167, 2, v164
	s_cmp_eq_u32 s12, 0
	s_cselect_b32 s23, 6, 64
	v_add_u32_e32 v168, 0, v167
	v_cmp_gt_u32_e32 vcc, s23, v168
	s_nop 1
	v_cndmask_b32_e64 v15, 0, 1.0, vcc
	v_add_u32_e32 v168, 1, v167
	v_cmp_gt_u32_e32 vcc, s23, v168
	s_nop 1
	v_cndmask_b32_e64 v16, 0, 1.0, vcc
	v_add_u32_e32 v168, 2, v167
	v_cmp_gt_u32_e32 vcc, s23, v168
	s_nop 1
	v_cndmask_b32_e64 v17, 0, 1.0, vcc
	v_add_u32_e32 v168, 3, v167
	v_cmp_gt_u32_e32 vcc, s23, v168
	s_nop 1
	v_cndmask_b32_e64 v18, 0, 1.0, vcc
	v_and_b32_e32 v167, 31, v8
	v_lshlrev_b32_e32 v167, 4, v167
	s_lshl_b32 s24, s12, 11
	s_add_i32 s25, s12, 7
	s_and_b32 s25, s25, 7
	s_lshl_b32 s26, s25, 11
	v_or_b32_e32 v4, s24, v167
	v_or_b32_e32 v5, s26, v167
	s_lshl_b32 s28, s25, 2
	s_add_u32 s28, s28, 0x10000
	v_mov_b32_e32 v7, s28
	v_mov_b32_e32 v19, 0
	v_mov_b32_e32 v20, 0
	v_mov_b32_e32 v21, 0
	v_mov_b32_e32 v22, 0
	s_waitcnt lgkmcnt(0)
	v_cmp_lt_u32_e64 s[32:33], 31, v8
	v_cmp_gt_u32_e64 s[34:35], 32, v8
	v_pack_b32_f16 v24, v188, v189
	v_pack_b32_f16 v25, v190, v191
	v_pack_b32_f16 v26, v192, v193
	v_pack_b32_f16 v27, v194, v195
	v_pack_b32_f16 v167, v196, v197
	v_cndmask_b32_e64 v28, 0, v167, s[32:33]
	v_cndmask_b32_e64 v32, 0, v167, s[34:35]
	v_pack_b32_f16 v167, v198, v199
	v_cndmask_b32_e64 v29, 0, v167, s[32:33]
	v_cndmask_b32_e64 v33, 0, v167, s[34:35]
	v_pack_b32_f16 v167, v200, v201
	v_cndmask_b32_e64 v30, 0, v167, s[32:33]
	v_cndmask_b32_e64 v34, 0, v167, s[34:35]
	v_pack_b32_f16 v167, v202, v203
	v_cndmask_b32_e64 v31, 0, v167, s[32:33]
	v_cndmask_b32_e64 v35, 0, v167, s[34:35]
	s_waitcnt lgkmcnt(0)
	s_cmp_lt_u32 s12, 4
	s_cbranch_scc1 .Lq_noprio
	s_setprio 1
